# baseline (speedup 1.0000x reference)
_Z11gemm_kernelPKfPKDF16bS0_Pf:
	s_and_b32 s3, s2, 7
	s_ashr_i32 s14, s2, 3
	s_lshl_b32 s12, s3, 6
	s_load_dwordx8 s[4:11], s[0:1], 0x0
	s_add_i32 s12, s12, s14
	s_bfe_u32 s18, s2, 0x10002
	s_lshl_b32 s2, s12, 6
	s_lshl_b32 s13, s18, 14
	s_and_b32 s2, s2, 0x3f00
	v_lshrrev_b32_e32 v52, 6, v0
	v_and_b32_e32 v50, 15, v0
	v_bfe_u32 v51, v0, 4, 2
	v_bfe_u32 v1, v0, 3, 3
	s_or_b32 s2, s2, s13
	v_lshl_or_b32 v102, v52, 2, v51
	v_lshl_or_b32 v104, v52, 3, v1
	v_lshlrev_b32_e32 v1, 4, v50
	s_lshl_b32 s15, s2, 9
	s_waitcnt lgkmcnt(0)
	s_mov_b32 s28, s10
	s_and_b32 s29, s11, 0xffff
	s_mov_b32 s30, 0x7fffffff
	s_mov_b32 s31, 0x20000
	v_and_b32_e32 v238, 3, v52
	v_lshlrev_b32_e32 v238, 6, v238
	v_lshl_or_b32 v238, v51, 2, v238
	v_lshlrev_b32_e32 v238, 2, v238
	s_and_b32 s24, s12, 3
	s_lshl_b32 s24, s24, 8
	s_lshl_b32 s25, s18, 10
	s_add_u32 s24, s24, s25
	s_lshl_b32 s24, s24, 2
	s_add_u32 s24, s8, s24
	s_addc_u32 s25, s9, 0
	global_load_dwordx4 v[240:243], v238, s[24:25]
	global_load_dwordx4 v[244:247], v238, s[24:25] offset:64
	global_load_dwordx4 v[248:251], v238, s[24:25] offset:128
	global_load_dwordx4 v[252:255], v238, s[24:25] offset:192
	s_mov_b64 s[0:1], s[6:7]
	s_and_b32 s5, s5, 0xffff
	s_mov_b32 s7, 0x20000
	s_brev_b32 s6, -2
	v_lshl_or_b32 v1, v102, 9, v1
	s_or_b32 s2, s15, 0x4000
	s_lshl_b32 s14, s14, 8
	v_lshlrev_b32_e32 v103, 3, v0
	buffer_load_dwordx4 v[54:57], v1, s[4:7], s15 offen sc0 nt
	buffer_load_dwordx4 v[58:61], v1, s[4:7], s2 offen sc0 nt
	s_or_b32 s2, s15, 0x8000
	s_or_b32 s3, s15, 0xc000
	s_lshl_b32 s19, s18, 10
	s_and_b32 s20, s14, 0x300
	v_and_b32_e32 v105, 56, v103
	buffer_load_dwordx4 v[62:65], v1, s[4:7], s2 offen sc0 nt
	buffer_load_dwordx4 v[66:69], v1, s[4:7], s3 offen sc0 nt
	s_or_b32 s2, s15, 0x10000
	s_or_b32 s3, s15, 0x14000
	s_or_b32 s14, s19, s20
	v_lshlrev_b32_e32 v106, 1, v105
	buffer_load_dwordx4 v[70:73], v1, s[4:7], s2 offen sc0 nt
	buffer_load_dwordx4 v[74:77], v1, s[4:7], s3 offen sc0 nt
	s_or_b32 s2, s15, 0x18000
	s_or_b32 s3, s15, 0x1c000
	s_lshl_b32 s14, s14, 11
	buffer_load_dwordx4 v[78:81], v1, s[4:7], s2 offen sc0 nt
	buffer_load_dwordx4 v[82:85], v1, s[4:7], s3 offen sc0 nt
	s_and_b32 s1, s1, 0xffff
	s_mov_b32 s2, s6
	s_mov_b32 s3, s7
	v_lshl_or_b32 v188, v104, 7, v106
	s_or_b32 s16, s14, 0x2000
	buffer_load_dwordx4 v[86:89], v188, s[0:3], s14 offen sc1
	buffer_load_dwordx4 v[90:93], v188, s[0:3], s16 offen sc1
	s_or_b32 s16, s14, 0x4000
	s_or_b32 s17, s14, 0x6000
	buffer_load_dwordx4 v[94:97], v188, s[0:3], s16 offen sc1
	buffer_load_dwordx4 v[98:101], v188, s[0:3], s17 offen sc1
	s_or_b32 s16, s15, 0x100
	s_or_b32 s17, s15, 0x4100
	buffer_load_dwordx4 v[10:13], v1, s[4:7], s16 offen sc0 nt
	buffer_load_dwordx4 v[18:21], v1, s[4:7], s17 offen sc0 nt
	s_or_b32 s16, s15, 0x8100
	s_or_b32 s17, s15, 0xc100
	buffer_load_dwordx4 v[22:25], v1, s[4:7], s16 offen sc0 nt
	buffer_load_dwordx4 v[30:33], v1, s[4:7], s17 offen sc0 nt
	s_or_b32 s16, s15, 0x10100
	s_or_b32 s17, s15, 0x14100
	buffer_load_dwordx4 v[34:37], v1, s[4:7], s16 offen sc0 nt
	buffer_load_dwordx4 v[38:41], v1, s[4:7], s17 offen sc0 nt
	s_or_b32 s16, s15, 0x18100
	s_or_b32 s15, s15, 0x1c100
	buffer_load_dwordx4 v[42:45], v1, s[4:7], s16 offen sc0 nt
	buffer_load_dwordx4 v[46:49], v1, s[4:7], s15 offen sc0 nt
	s_or_b32 s15, s14, 0x8000
	s_or_b32 s16, s14, 0xa000
	buffer_load_dwordx4 v[2:5], v188, s[0:3], s15 offen sc1
	buffer_load_dwordx4 v[6:9], v188, s[0:3], s16 offen sc1
	s_or_b32 s15, s14, 0xc000
	s_or_b32 s16, s14, 0xe000
	buffer_load_dwordx4 v[14:17], v188, s[0:3], s15 offen sc1
	buffer_load_dwordx4 v[26:29], v188, s[0:3], s16 offen sc1
	v_lshrrev_b32_e32 v107, 7, v0
	v_bfe_u32 v108, v0, 3, 1
	v_lshlrev_b32_e32 v102, 6, v102
	s_movk_i32 s2, 0x3c0
	v_and_or_b32 v102, v102, s2, v105
	v_lshrrev_b32_e32 v105, 2, v0
	v_and_or_b32 v107, v107, 2, v108
	v_and_b32_e32 v105, 32, v105
	v_lshlrev_b32_e32 v107, 10, v107
	v_bfe_u32 v103, v103, 5, 1
	v_lshlrev_b32_e32 v104, 6, v104
	v_and_b32_e32 v106, 48, v106
	v_bitop3_b32 v189, v102, v107, v105 bitop3:0xde
	v_and_or_b32 v103, v52, 6, v103
	v_and_or_b32 v104, v104, s2, v106
	v_lshrrev_b32_e32 v106, 1, v0
	v_lshlrev_b32_e32 v103, 10, v103
	v_and_b32_e32 v106, 32, v106
	v_bitop3_b32 v190, v104, v103, v106 bitop3:0xde
	v_lshrrev_b32_e32 v53, 8, v0
	s_movk_i32 s15, 0x4000
	s_mov_b32 s16, 0x8000
	s_mov_b32 s17, 0xc000
	s_waitcnt vmcnt(23)
	v_cvt_pk_bf16_f32 v57, v56, v57
	v_cvt_pk_bf16_f32 v56, v54, v55
	s_waitcnt vmcnt(22)
	v_cvt_pk_bf16_f32 v55, v60, v61
	v_cvt_pk_bf16_f32 v54, v58, v59
	ds_write2st64_b64 v189, v[56:57], v[54:55] offset1:8
	s_waitcnt vmcnt(21)
	v_cvt_pk_bf16_f32 v55, v64, v65
	v_cvt_pk_bf16_f32 v54, v62, v63
	s_waitcnt vmcnt(20)
	v_cvt_pk_bf16_f32 v57, v68, v69
	v_cvt_pk_bf16_f32 v56, v66, v67
	ds_write2st64_b64 v189, v[54:55], v[56:57] offset0:16 offset1:24
	s_waitcnt vmcnt(19)
	v_cvt_pk_bf16_f32 v55, v72, v73
	v_cvt_pk_bf16_f32 v54, v70, v71
	s_waitcnt vmcnt(18)
	v_cvt_pk_bf16_f32 v57, v76, v77
	v_cvt_pk_bf16_f32 v56, v74, v75
	ds_write2st64_b64 v189, v[54:55], v[56:57] offset0:32 offset1:40
	s_waitcnt vmcnt(17)
	v_cvt_pk_bf16_f32 v55, v80, v81
	v_cvt_pk_bf16_f32 v54, v78, v79
	s_waitcnt vmcnt(16)
	v_cvt_pk_bf16_f32 v57, v84, v85
	v_cvt_pk_bf16_f32 v56, v82, v83
	ds_write2st64_b64 v189, v[54:55], v[56:57] offset0:48 offset1:56
	s_waitcnt vmcnt(15)
	ds_write_b128 v190, v[86:89] offset:32768
	s_waitcnt vmcnt(14)
	ds_write_b128 v190, v[90:93] offset:40960
	s_waitcnt vmcnt(13)
	ds_write_b128 v190, v[94:97] offset:49152
	s_waitcnt vmcnt(12)
	ds_write_b128 v190, v[98:101] offset:57344
	s_waitcnt lgkmcnt(0)
	s_barrier
	v_cmp_eq_u32_e32 vcc, 1, v53
	s_and_saveexec_b64 s[2:3], vcc
	s_cbranch_execz .LBB1_2
	s_barrier
.LBB1_2:
	s_or_b64 exec, exec, s[2:3]
	v_and_b32_e32 v52, 3, v52
	v_and_b32_e32 v54, 48, v0
	v_lshlrev_b32_e32 v55, 2, v0
	v_lshl_or_b32 v54, v50, 6, v54
	v_and_b32_e32 v55, 32, v55
	v_lshlrev_b32_e32 v56, 14, v53
	v_lshlrev_b32_e32 v57, 13, v52
	v_lshl_or_b32 v52, v52, 6, s20
	v_lshlrev_b32_e32 v51, 2, v51
	s_movk_i32 s2, 0x4c
	v_bitop3_b32 v191, v54, v57, v55 bitop3:0xde
	v_bitop3_b32 v192, v54, v56, v55 bitop3:0xde
	v_or_b32_e32 v54, v52, v51
	v_bitop3_b32 v51, v52, s2, v51 bitop3:0xc8
	v_lshrrev_b32_e32 v52, 6, v52
	s_lshl_b32 s2, s19, 2
	v_and_or_b32 v52, v52, 14, s18
	v_lshlrev_b32_e32 v182, 2, v51
	v_mov_b32_e32 v183, 0
	s_add_u32 s2, s8, s2
	v_lshlrev_b32_e32 v52, 14, v52
	v_lshlrev_b32_e32 v53, 7, v53
	v_mov_b32_e32 v184, v182
	s_addc_u32 s3, s9, 0
	v_lshlrev_b32_e32 v182, 2, v54
	v_or3_b32 v193, v53, v52, v50
	s_mov_b32 s18, 0
	v_lshl_add_u64 v[186:187], s[2:3], 0, v[182:183]
	s_mov_b32 s2, s6
	s_mov_b32 s3, s7
	s_movk_i32 s8, 0x2000
	s_movk_i32 s9, 0x6000
	s_mov_b32 s10, 0xa000
	s_mov_b32 s11, 0xe000
	s_mov_b32 s19, 0
	s_mov_b32 s20, 0
	s_branch .Lfirst

.LBB1_4:
	v_add_u32_e32 v182, s19, v191
	v_add_u32_e32 v238, s19, v192
	ds_read_b128 v[178:181], v182 offset:32768
	ds_read_b128 v[194:197], v182 offset:34816
	ds_read_b128 v[198:201], v182 offset:36864
	ds_read_b128 v[202:205], v182 offset:38912
	ds_read_b128 v[206:209], v238
	ds_read_b128 v[210:213], v238 offset:2048
	ds_read_b128 v[214:217], v238 offset:4096
	ds_read_b128 v[218:221], v238 offset:6144
	ds_read_b128 v[222:225], v238 offset:8192
	ds_read_b128 v[226:229], v238 offset:10240
	ds_read_b128 v[230:233], v238 offset:12288
	ds_read_b128 v[234:237], v238 offset:14336
	s_min_u32 s21, s20, 29
	s_xor_b32 s19, s19, 0x10000
	v_add_u32_e32 v239, s19, v189
	s_waitcnt vmcnt(11)
	v_cvt_pk_bf16_f32 v13, v12, v13
	v_cvt_pk_bf16_f32 v12, v10, v11
	s_waitcnt vmcnt(10)
	v_cvt_pk_bf16_f32 v11, v20, v21
	v_cvt_pk_bf16_f32 v10, v18, v19
	ds_write2st64_b64 v239, v[12:13], v[10:11] offset1:8
	s_waitcnt vmcnt(9)
	v_cvt_pk_bf16_f32 v11, v24, v25
	v_cvt_pk_bf16_f32 v10, v22, v23
	s_waitcnt vmcnt(8)
	v_cvt_pk_bf16_f32 v13, v32, v33
	v_cvt_pk_bf16_f32 v12, v30, v31
	ds_write2st64_b64 v239, v[10:11], v[12:13] offset0:16 offset1:24
	s_waitcnt vmcnt(7)
	v_cvt_pk_bf16_f32 v11, v36, v37
	v_cvt_pk_bf16_f32 v10, v34, v35
	s_waitcnt vmcnt(6)
	v_cvt_pk_bf16_f32 v13, v40, v41
	v_cvt_pk_bf16_f32 v12, v38, v39
	ds_write2st64_b64 v239, v[10:11], v[12:13] offset0:32 offset1:40
	s_waitcnt vmcnt(5)
	v_cvt_pk_bf16_f32 v11, v44, v45
	v_cvt_pk_bf16_f32 v10, v42, v43
	s_waitcnt vmcnt(4)
	v_cvt_pk_bf16_f32 v13, v48, v49
	v_cvt_pk_bf16_f32 v12, v46, v47
	ds_write2st64_b64 v239, v[10:11], v[12:13] offset0:48 offset1:56
	s_waitcnt lgkmcnt(0)
	s_add_i32 s21, s21, 2
	s_barrier
	s_waitcnt lgkmcnt(11)
	v_mfma_f32_16x16x32_bf16 v[174:177], v[178:181], v[206:209], v[174:177]
	s_lshl_b32 s22, s21, 1
	s_and_b32 s22, s22, 0x60
	s_add_i32 s22, s22, s12
	s_lshl_b32 s22, s22, 6
	v_mfma_f32_16x16x32_bf16 v[170:173], v[194:197], v[206:209], v[170:173]
	s_and_b32 s22, s22, 0x3f00
	s_or_b32 s22, s22, s13
	s_lshl_b32 s23, s21, 23
	s_lshl_b32 s22, s22, 9
	v_mfma_f32_16x16x32_bf16 v[158:161], v[198:201], v[206:209], v[158:161]
	s_and_b32 s23, s23, 0x7000000
	s_or_b32 s22, s22, s23
	s_lshl_b32 s23, s21, 8
	s_and_b32 s23, s23, 0x100
	s_or_b32 s22, s22, s23
	s_or_b32 s23, s22, 0x4000
	buffer_load_dwordx4 v[10:13], v1, s[4:7], s22 offen sc0 nt
	v_mfma_f32_16x16x32_bf16 v[142:145], v[202:205], v[206:209], v[142:145]
	s_waitcnt lgkmcnt(10)
	v_mfma_f32_16x16x32_bf16 v[166:169], v[178:181], v[210:213], v[166:169]
	v_mfma_f32_16x16x32_bf16 v[162:165], v[194:197], v[210:213], v[162:165]
	v_mfma_f32_16x16x32_bf16 v[146:149], v[198:201], v[210:213], v[146:149]
	buffer_load_dwordx4 v[18:21], v1, s[4:7], s23 offen sc0 nt
	s_or_b32 s23, s22, 0x8000
	v_mfma_f32_16x16x32_bf16 v[122:125], v[202:205], v[210:213], v[122:125]
	s_waitcnt lgkmcnt(9)
	v_mfma_f32_16x16x32_bf16 v[154:157], v[178:181], v[214:217], v[154:157]
	v_mfma_f32_16x16x32_bf16 v[150:153], v[194:197], v[214:217], v[150:153]
	v_mfma_f32_16x16x32_bf16 v[130:133], v[198:201], v[214:217], v[130:133]
	buffer_load_dwordx4 v[22:25], v1, s[4:7], s23 offen sc0 nt
	s_or_b32 s23, s22, 0xc000
	v_mfma_f32_16x16x32_bf16 v[106:109], v[202:205], v[214:217], v[106:109]
	s_waitcnt lgkmcnt(8)
	v_mfma_f32_16x16x32_bf16 v[138:141], v[178:181], v[218:221], v[138:141]
	v_mfma_f32_16x16x32_bf16 v[134:137], v[194:197], v[218:221], v[134:137]
	v_mfma_f32_16x16x32_bf16 v[114:117], v[198:201], v[218:221], v[114:117]
	buffer_load_dwordx4 v[30:33], v1, s[4:7], s23 offen sc0 nt
	s_or_b32 s23, s22, 0x10000
	v_mfma_f32_16x16x32_bf16 v[90:93], v[202:205], v[218:221], v[90:93]
	s_waitcnt lgkmcnt(7)
	v_mfma_f32_16x16x32_bf16 v[126:129], v[178:181], v[222:225], v[126:129]
	v_mfma_f32_16x16x32_bf16 v[118:121], v[194:197], v[222:225], v[118:121]
	v_mfma_f32_16x16x32_bf16 v[98:101], v[198:201], v[222:225], v[98:101]
	buffer_load_dwordx4 v[34:37], v1, s[4:7], s23 offen sc0 nt
	s_or_b32 s23, s22, 0x14000
	v_mfma_f32_16x16x32_bf16 v[74:77], v[202:205], v[222:225], v[74:77]
	s_waitcnt lgkmcnt(6)
	v_mfma_f32_16x16x32_bf16 v[110:113], v[178:181], v[226:229], v[110:113]
	v_mfma_f32_16x16x32_bf16 v[102:105], v[194:197], v[226:229], v[102:105]
	v_mfma_f32_16x16x32_bf16 v[82:85], v[198:201], v[226:229], v[82:85]
	buffer_load_dwordx4 v[38:41], v1, s[4:7], s23 offen sc0 nt
	s_or_b32 s23, s22, 0x18000
	s_or_b32 s22, s22, 0x1c000
	v_mfma_f32_16x16x32_bf16 v[62:65], v[202:205], v[226:229], v[62:65]
	s_waitcnt lgkmcnt(5)
	v_mfma_f32_16x16x32_bf16 v[94:97], v[178:181], v[230:233], v[94:97]
	v_mfma_f32_16x16x32_bf16 v[86:89], v[194:197], v[230:233], v[86:89]
	v_mfma_f32_16x16x32_bf16 v[70:73], v[198:201], v[230:233], v[70:73]
	buffer_load_dwordx4 v[42:45], v1, s[4:7], s23 offen sc0 nt
	v_mfma_f32_16x16x32_bf16 v[54:57], v[202:205], v[230:233], v[54:57]
	s_waitcnt lgkmcnt(4)
	v_mfma_f32_16x16x32_bf16 v[78:81], v[178:181], v[234:237], v[78:81]
	v_mfma_f32_16x16x32_bf16 v[66:69], v[194:197], v[234:237], v[66:69]
	v_mfma_f32_16x16x32_bf16 v[58:61], v[198:201], v[234:237], v[58:61]
	buffer_load_dwordx4 v[46:49], v1, s[4:7], s22 offen sc0 nt
	v_mfma_f32_16x16x32_bf16 v[50:53], v[202:205], v[234:237], v[50:53]
	s_waitcnt lgkmcnt(0)
	s_barrier
	ds_read_b128 v[178:181], v182 offset:33792
	ds_read_b128 v[194:197], v182 offset:35840
	ds_read_b128 v[198:201], v182 offset:37888
	ds_read_b128 v[202:205], v182 offset:39936
	ds_read_b128 v[206:209], v238 offset:1024
	ds_read_b128 v[210:213], v238 offset:3072
	ds_read_b128 v[214:217], v238 offset:5120
	ds_read_b128 v[218:221], v238 offset:7168
	ds_read_b128 v[222:225], v238 offset:9216
	ds_read_b128 v[226:229], v238 offset:11264
	ds_read_b128 v[230:233], v238 offset:13312
	ds_read_b128 v[234:237], v238 offset:15360
	v_add_u32_e32 v182, s19, v190
	s_waitcnt vmcnt(11)
	ds_write_b128 v182, v[2:5] offset:32768
	s_waitcnt vmcnt(10)
	ds_write_b128 v182, v[6:9] offset:40960
	s_waitcnt vmcnt(9)
	ds_write_b128 v182, v[14:17] offset:49152
	s_waitcnt vmcnt(8)
	ds_write_b128 v182, v[26:29] offset:57344
	s_waitcnt lgkmcnt(0)
	s_barrier
	s_waitcnt lgkmcnt(11)
	v_mfma_f32_16x16x32_bf16 v[174:177], v[178:181], v[206:209], v[174:177]
	s_lshl_b32 s21, s21, 15
	s_and_b32 s21, s21, 0x78000
	s_or_b32 s21, s21, s14
	s_or_b32 s22, s21, 0x2000
	v_mfma_f32_16x16x32_bf16 v[170:173], v[194:197], v[206:209], v[170:173]
	v_mfma_f32_16x16x32_bf16 v[158:161], v[198:201], v[206:209], v[158:161]
	v_mfma_f32_16x16x32_bf16 v[142:145], v[202:205], v[206:209], v[142:145]
	s_waitcnt lgkmcnt(10)
	v_mfma_f32_16x16x32_bf16 v[166:169], v[178:181], v[210:213], v[166:169]
	v_mfma_f32_16x16x32_bf16 v[162:165], v[194:197], v[210:213], v[162:165]
	buffer_load_dwordx4 v[2:5], v188, s[0:3], s21 offen sc1
	v_mfma_f32_16x16x32_bf16 v[146:149], v[198:201], v[210:213], v[146:149]
	v_mfma_f32_16x16x32_bf16 v[122:125], v[202:205], v[210:213], v[122:125]
	s_waitcnt lgkmcnt(9)
	v_mfma_f32_16x16x32_bf16 v[154:157], v[178:181], v[214:217], v[154:157]
	v_mfma_f32_16x16x32_bf16 v[150:153], v[194:197], v[214:217], v[150:153]
	v_mfma_f32_16x16x32_bf16 v[130:133], v[198:201], v[214:217], v[130:133]
	v_mfma_f32_16x16x32_bf16 v[106:109], v[202:205], v[214:217], v[106:109]
	s_waitcnt lgkmcnt(8)
	v_mfma_f32_16x16x32_bf16 v[138:141], v[178:181], v[218:221], v[138:141]
	v_mfma_f32_16x16x32_bf16 v[134:137], v[194:197], v[218:221], v[134:137]
	buffer_load_dwordx4 v[6:9], v188, s[0:3], s22 offen sc1
	s_or_b32 s22, s21, 0x4000
	s_or_b32 s21, s21, 0x6000
	v_mfma_f32_16x16x32_bf16 v[114:117], v[198:201], v[218:221], v[114:117]
	v_mfma_f32_16x16x32_bf16 v[90:93], v[202:205], v[218:221], v[90:93]
	s_waitcnt lgkmcnt(7)
	v_mfma_f32_16x16x32_bf16 v[126:129], v[178:181], v[222:225], v[126:129]
	v_mfma_f32_16x16x32_bf16 v[118:121], v[194:197], v[222:225], v[118:121]
	v_mfma_f32_16x16x32_bf16 v[98:101], v[198:201], v[222:225], v[98:101]
	v_mfma_f32_16x16x32_bf16 v[74:77], v[202:205], v[222:225], v[74:77]
	s_waitcnt lgkmcnt(6)
	v_mfma_f32_16x16x32_bf16 v[110:113], v[178:181], v[226:229], v[110:113]
	v_mfma_f32_16x16x32_bf16 v[102:105], v[194:197], v[226:229], v[102:105]
	buffer_load_dwordx4 v[14:17], v188, s[0:3], s22 offen sc1
	v_mfma_f32_16x16x32_bf16 v[82:85], v[198:201], v[226:229], v[82:85]
	v_mfma_f32_16x16x32_bf16 v[62:65], v[202:205], v[226:229], v[62:65]
	s_waitcnt lgkmcnt(5)
	v_mfma_f32_16x16x32_bf16 v[94:97], v[178:181], v[230:233], v[94:97]
	v_mfma_f32_16x16x32_bf16 v[86:89], v[194:197], v[230:233], v[86:89]
	v_mfma_f32_16x16x32_bf16 v[70:73], v[198:201], v[230:233], v[70:73]
	v_mfma_f32_16x16x32_bf16 v[54:57], v[202:205], v[230:233], v[54:57]
	s_waitcnt lgkmcnt(4)
	v_mfma_f32_16x16x32_bf16 v[78:81], v[178:181], v[234:237], v[78:81]
	v_mfma_f32_16x16x32_bf16 v[66:69], v[194:197], v[234:237], v[66:69]
	buffer_load_dwordx4 v[26:29], v188, s[0:3], s21 offen sc1
	v_mfma_f32_16x16x32_bf16 v[58:61], v[198:201], v[234:237], v[58:61]
	v_mfma_f32_16x16x32_bf16 v[50:53], v[202:205], v[234:237], v[50:53]
	s_and_b32 s21, s20, 15
	s_cmp_lg_u32 s21, 15
	s_cbranch_scc1 .LBB1_3
	s_and_b32 s21, s18, 32
	s_add_i32 s21, s21, s12
	s_lshl_b32 s21, s21, 6
	s_and_b32 s21, s21, 0x3f00
	v_add_lshl_u32 v182, v193, s21, 9
	v_add_u32_e32 v206, v184, v182
	buffer_store_dwordx4 v[174:177], v206, s[28:31], 0 offen
	buffer_store_dwordx4 v[170:173], v206, s[28:31], 0 offen offset:64
	buffer_store_dwordx4 v[158:161], v206, s[28:31], 0 offen offset:128
	buffer_store_dwordx4 v[142:145], v206, s[28:31], 0 offen offset:192
	buffer_store_dwordx4 v[166:169], v206, s[28:31], s8 offen
	buffer_store_dwordx4 v[162:165], v206, s[28:31], s8 offen offset:64
	buffer_store_dwordx4 v[146:149], v206, s[28:31], s8 offen offset:128
	buffer_store_dwordx4 v[122:125], v206, s[28:31], s8 offen offset:192
	buffer_store_dwordx4 v[154:157], v206, s[28:31], s15 offen
	buffer_store_dwordx4 v[150:153], v206, s[28:31], s15 offen offset:64
	buffer_store_dwordx4 v[130:133], v206, s[28:31], s15 offen offset:128
	buffer_store_dwordx4 v[106:109], v206, s[28:31], s15 offen offset:192
	buffer_store_dwordx4 v[138:141], v206, s[28:31], s9 offen
	buffer_store_dwordx4 v[134:137], v206, s[28:31], s9 offen offset:64
	buffer_store_dwordx4 v[114:117], v206, s[28:31], s9 offen offset:128
	buffer_store_dwordx4 v[90:93], v206, s[28:31], s9 offen offset:192
	buffer_store_dwordx4 v[126:129], v206, s[28:31], s16 offen
	buffer_store_dwordx4 v[118:121], v206, s[28:31], s16 offen offset:64
	buffer_store_dwordx4 v[98:101], v206, s[28:31], s16 offen offset:128
	buffer_store_dwordx4 v[74:77], v206, s[28:31], s16 offen offset:192
	buffer_store_dwordx4 v[110:113], v206, s[28:31], s10 offen
	buffer_store_dwordx4 v[102:105], v206, s[28:31], s10 offen offset:64
	buffer_store_dwordx4 v[82:85], v206, s[28:31], s10 offen offset:128
	buffer_store_dwordx4 v[62:65], v206, s[28:31], s10 offen offset:192
	buffer_store_dwordx4 v[94:97], v206, s[28:31], s17 offen
	buffer_store_dwordx4 v[86:89], v206, s[28:31], s17 offen offset:64
	buffer_store_dwordx4 v[70:73], v206, s[28:31], s17 offen offset:128
	buffer_store_dwordx4 v[54:57], v206, s[28:31], s17 offen offset:192
	buffer_store_dwordx4 v[78:81], v206, s[28:31], s11 offen
	buffer_store_dwordx4 v[66:69], v206, s[28:31], s11 offen offset:64
	buffer_store_dwordx4 v[58:61], v206, s[28:31], s11 offen offset:128
	buffer_store_dwordx4 v[50:53], v206, s[28:31], s11 offen offset:192

.Lt30:
	v_add_u32_e32 v182, s19, v191
	v_add_u32_e32 v238, s19, v192
	ds_read_b128 v[178:181], v182 offset:32768
	ds_read_b128 v[194:197], v182 offset:34816
	ds_read_b128 v[198:201], v182 offset:36864
	ds_read_b128 v[202:205], v182 offset:38912
	ds_read_b128 v[206:209], v238
	ds_read_b128 v[210:213], v238 offset:2048
	ds_read_b128 v[214:217], v238 offset:4096
	ds_read_b128 v[218:221], v238 offset:6144
	ds_read_b128 v[222:225], v238 offset:8192
	ds_read_b128 v[226:229], v238 offset:10240
	ds_read_b128 v[230:233], v238 offset:12288
	ds_read_b128 v[234:237], v238 offset:14336
	s_min_u32 s21, s20, 29
	s_xor_b32 s19, s19, 0x10000
	v_add_u32_e32 v239, s19, v189
	s_waitcnt vmcnt(11)
	v_cvt_pk_bf16_f32 v13, v12, v13
	v_cvt_pk_bf16_f32 v12, v10, v11
	s_waitcnt vmcnt(10)
	v_cvt_pk_bf16_f32 v11, v20, v21
	v_cvt_pk_bf16_f32 v10, v18, v19
	ds_write2st64_b64 v239, v[12:13], v[10:11] offset1:8
	s_waitcnt vmcnt(9)
	v_cvt_pk_bf16_f32 v11, v24, v25
	v_cvt_pk_bf16_f32 v10, v22, v23
	s_waitcnt vmcnt(8)
	v_cvt_pk_bf16_f32 v13, v32, v33
	v_cvt_pk_bf16_f32 v12, v30, v31
	ds_write2st64_b64 v239, v[10:11], v[12:13] offset0:16 offset1:24
	s_waitcnt vmcnt(7)
	v_cvt_pk_bf16_f32 v11, v36, v37
	v_cvt_pk_bf16_f32 v10, v34, v35
	s_waitcnt vmcnt(6)
	v_cvt_pk_bf16_f32 v13, v40, v41
	v_cvt_pk_bf16_f32 v12, v38, v39
	ds_write2st64_b64 v239, v[10:11], v[12:13] offset0:32 offset1:40
	s_waitcnt vmcnt(5)
	v_cvt_pk_bf16_f32 v11, v44, v45
	v_cvt_pk_bf16_f32 v10, v42, v43
	s_waitcnt vmcnt(4)
	v_cvt_pk_bf16_f32 v13, v48, v49
	v_cvt_pk_bf16_f32 v12, v46, v47
	ds_write2st64_b64 v239, v[10:11], v[12:13] offset0:48 offset1:56
	s_waitcnt lgkmcnt(0)
	s_add_i32 s21, s21, 2
	s_barrier
	s_waitcnt lgkmcnt(11)
	v_mfma_f32_16x16x32_bf16 v[174:177], v[178:181], v[206:209], v[174:177]
	s_lshl_b32 s22, s21, 1
	s_and_b32 s22, s22, 0x60
	s_add_i32 s22, s22, s12
	s_lshl_b32 s22, s22, 6
	v_mfma_f32_16x16x32_bf16 v[170:173], v[194:197], v[206:209], v[170:173]
	s_and_b32 s22, s22, 0x3f00
	s_or_b32 s22, s22, s13
	s_lshl_b32 s23, s21, 23
	s_lshl_b32 s22, s22, 9
	v_mfma_f32_16x16x32_bf16 v[158:161], v[198:201], v[206:209], v[158:161]
	s_and_b32 s23, s23, 0x7000000
	s_or_b32 s22, s22, s23
	s_lshl_b32 s23, s21, 8
	s_and_b32 s23, s23, 0x100
	s_or_b32 s22, s22, s23
	s_or_b32 s23, s22, 0x4000
	v_mfma_f32_16x16x32_bf16 v[142:145], v[202:205], v[206:209], v[142:145]
	s_waitcnt lgkmcnt(10)
	v_mfma_f32_16x16x32_bf16 v[166:169], v[178:181], v[210:213], v[166:169]
	v_mfma_f32_16x16x32_bf16 v[162:165], v[194:197], v[210:213], v[162:165]
	v_mfma_f32_16x16x32_bf16 v[146:149], v[198:201], v[210:213], v[146:149]
	s_or_b32 s23, s22, 0x8000
	v_mfma_f32_16x16x32_bf16 v[122:125], v[202:205], v[210:213], v[122:125]
	s_waitcnt lgkmcnt(9)
	v_mfma_f32_16x16x32_bf16 v[154:157], v[178:181], v[214:217], v[154:157]
	v_mfma_f32_16x16x32_bf16 v[150:153], v[194:197], v[214:217], v[150:153]
	v_mfma_f32_16x16x32_bf16 v[130:133], v[198:201], v[214:217], v[130:133]
	s_or_b32 s23, s22, 0xc000
	v_mfma_f32_16x16x32_bf16 v[106:109], v[202:205], v[214:217], v[106:109]
	s_waitcnt lgkmcnt(8)
	v_mfma_f32_16x16x32_bf16 v[138:141], v[178:181], v[218:221], v[138:141]
	v_mfma_f32_16x16x32_bf16 v[134:137], v[194:197], v[218:221], v[134:137]
	v_mfma_f32_16x16x32_bf16 v[114:117], v[198:201], v[218:221], v[114:117]
	s_or_b32 s23, s22, 0x10000
	v_mfma_f32_16x16x32_bf16 v[90:93], v[202:205], v[218:221], v[90:93]
	s_waitcnt lgkmcnt(7)
	v_mfma_f32_16x16x32_bf16 v[126:129], v[178:181], v[222:225], v[126:129]
	v_mfma_f32_16x16x32_bf16 v[118:121], v[194:197], v[222:225], v[118:121]
	v_mfma_f32_16x16x32_bf16 v[98:101], v[198:201], v[222:225], v[98:101]
	s_or_b32 s23, s22, 0x14000
	v_mfma_f32_16x16x32_bf16 v[74:77], v[202:205], v[222:225], v[74:77]
	s_waitcnt lgkmcnt(6)
	v_mfma_f32_16x16x32_bf16 v[110:113], v[178:181], v[226:229], v[110:113]
	v_mfma_f32_16x16x32_bf16 v[102:105], v[194:197], v[226:229], v[102:105]
	v_mfma_f32_16x16x32_bf16 v[82:85], v[198:201], v[226:229], v[82:85]
	s_or_b32 s23, s22, 0x18000
	s_or_b32 s22, s22, 0x1c000
	v_mfma_f32_16x16x32_bf16 v[62:65], v[202:205], v[226:229], v[62:65]
	s_waitcnt lgkmcnt(5)
	v_mfma_f32_16x16x32_bf16 v[94:97], v[178:181], v[230:233], v[94:97]
	v_mfma_f32_16x16x32_bf16 v[86:89], v[194:197], v[230:233], v[86:89]
	v_mfma_f32_16x16x32_bf16 v[70:73], v[198:201], v[230:233], v[70:73]
	v_mfma_f32_16x16x32_bf16 v[54:57], v[202:205], v[230:233], v[54:57]
	s_waitcnt lgkmcnt(4)
	v_mfma_f32_16x16x32_bf16 v[78:81], v[178:181], v[234:237], v[78:81]
	v_mfma_f32_16x16x32_bf16 v[66:69], v[194:197], v[234:237], v[66:69]
	v_mfma_f32_16x16x32_bf16 v[58:61], v[198:201], v[234:237], v[58:61]
	v_mfma_f32_16x16x32_bf16 v[50:53], v[202:205], v[234:237], v[50:53]
	s_waitcnt lgkmcnt(0)
	s_barrier
	ds_read_b128 v[178:181], v182 offset:33792
	ds_read_b128 v[194:197], v182 offset:35840
	ds_read_b128 v[198:201], v182 offset:37888
	ds_read_b128 v[202:205], v182 offset:39936
	ds_read_b128 v[206:209], v238 offset:1024
	ds_read_b128 v[210:213], v238 offset:3072
	ds_read_b128 v[214:217], v238 offset:5120
	ds_read_b128 v[218:221], v238 offset:7168
	ds_read_b128 v[222:225], v238 offset:9216
	ds_read_b128 v[226:229], v238 offset:11264
	ds_read_b128 v[230:233], v238 offset:13312
	ds_read_b128 v[234:237], v238 offset:15360
	v_add_u32_e32 v182, s19, v190
	s_waitcnt vmcnt(3)
	ds_write_b128 v182, v[2:5] offset:32768
	s_waitcnt vmcnt(2)
	ds_write_b128 v182, v[6:9] offset:40960
	s_waitcnt vmcnt(1)
	ds_write_b128 v182, v[14:17] offset:49152
	s_waitcnt vmcnt(0)
	ds_write_b128 v182, v[26:29] offset:57344
	s_waitcnt lgkmcnt(0)
	s_barrier
	s_waitcnt lgkmcnt(11)
	v_mfma_f32_16x16x32_bf16 v[174:177], v[178:181], v[206:209], v[174:177]
	s_lshl_b32 s21, s21, 15
	s_and_b32 s21, s21, 0x78000
	s_or_b32 s21, s21, s14
	s_or_b32 s22, s21, 0x2000
	v_mfma_f32_16x16x32_bf16 v[170:173], v[194:197], v[206:209], v[170:173]
	v_mfma_f32_16x16x32_bf16 v[158:161], v[198:201], v[206:209], v[158:161]
	v_mfma_f32_16x16x32_bf16 v[142:145], v[202:205], v[206:209], v[142:145]
	s_waitcnt lgkmcnt(10)
	v_mfma_f32_16x16x32_bf16 v[166:169], v[178:181], v[210:213], v[166:169]
	v_mfma_f32_16x16x32_bf16 v[162:165], v[194:197], v[210:213], v[162:165]
	v_mfma_f32_16x16x32_bf16 v[146:149], v[198:201], v[210:213], v[146:149]
	v_mfma_f32_16x16x32_bf16 v[122:125], v[202:205], v[210:213], v[122:125]
	s_waitcnt lgkmcnt(9)
	v_mfma_f32_16x16x32_bf16 v[154:157], v[178:181], v[214:217], v[154:157]
	v_mfma_f32_16x16x32_bf16 v[150:153], v[194:197], v[214:217], v[150:153]
	v_mfma_f32_16x16x32_bf16 v[130:133], v[198:201], v[214:217], v[130:133]
	v_mfma_f32_16x16x32_bf16 v[106:109], v[202:205], v[214:217], v[106:109]
	s_waitcnt lgkmcnt(8)
	v_mfma_f32_16x16x32_bf16 v[138:141], v[178:181], v[218:221], v[138:141]
	v_mfma_f32_16x16x32_bf16 v[134:137], v[194:197], v[218:221], v[134:137]
	s_or_b32 s22, s21, 0x4000
	s_or_b32 s21, s21, 0x6000
	v_mfma_f32_16x16x32_bf16 v[114:117], v[198:201], v[218:221], v[114:117]
	v_mfma_f32_16x16x32_bf16 v[90:93], v[202:205], v[218:221], v[90:93]
	s_waitcnt lgkmcnt(7)
	v_mfma_f32_16x16x32_bf16 v[126:129], v[178:181], v[222:225], v[126:129]
	v_mfma_f32_16x16x32_bf16 v[118:121], v[194:197], v[222:225], v[118:121]
	v_mfma_f32_16x16x32_bf16 v[98:101], v[198:201], v[222:225], v[98:101]
	v_mfma_f32_16x16x32_bf16 v[74:77], v[202:205], v[222:225], v[74:77]
	s_waitcnt lgkmcnt(6)
	v_mfma_f32_16x16x32_bf16 v[110:113], v[178:181], v[226:229], v[110:113]
	v_mfma_f32_16x16x32_bf16 v[102:105], v[194:197], v[226:229], v[102:105]
	v_mfma_f32_16x16x32_bf16 v[82:85], v[198:201], v[226:229], v[82:85]
	v_mfma_f32_16x16x32_bf16 v[62:65], v[202:205], v[226:229], v[62:65]
	s_waitcnt lgkmcnt(5)
	v_mfma_f32_16x16x32_bf16 v[94:97], v[178:181], v[230:233], v[94:97]
	v_mfma_f32_16x16x32_bf16 v[86:89], v[194:197], v[230:233], v[86:89]
	v_mfma_f32_16x16x32_bf16 v[70:73], v[198:201], v[230:233], v[70:73]
	v_mfma_f32_16x16x32_bf16 v[54:57], v[202:205], v[230:233], v[54:57]
	s_waitcnt lgkmcnt(4)
	v_mfma_f32_16x16x32_bf16 v[78:81], v[178:181], v[234:237], v[78:81]
	v_mfma_f32_16x16x32_bf16 v[66:69], v[194:197], v[234:237], v[66:69]
	v_mfma_f32_16x16x32_bf16 v[58:61], v[198:201], v[234:237], v[58:61]
	v_mfma_f32_16x16x32_bf16 v[50:53], v[202:205], v[234:237], v[50:53]
	s_waitcnt lgkmcnt(0)
	s_barrier
	s_add_i32 s20, s20, 1
	s_add_i32 s18, s18, 2
	v_add_u32_e32 v182, s19, v191
	v_add_u32_e32 v238, s19, v192
	ds_read_b128 v[178:181], v182 offset:32768
	ds_read_b128 v[194:197], v182 offset:34816
	ds_read_b128 v[198:201], v182 offset:36864
	ds_read_b128 v[202:205], v182 offset:38912
	ds_read_b128 v[206:209], v238
	ds_read_b128 v[210:213], v238 offset:2048
	ds_read_b128 v[214:217], v238 offset:4096
	ds_read_b128 v[218:221], v238 offset:6144
	ds_read_b128 v[222:225], v238 offset:8192
	ds_read_b128 v[226:229], v238 offset:10240
	ds_read_b128 v[230:233], v238 offset:12288
	ds_read_b128 v[234:237], v238 offset:14336
	s_min_u32 s21, s20, 29
	s_xor_b32 s19, s19, 0x10000
	v_add_u32_e32 v239, s19, v189
	s_waitcnt lgkmcnt(0)
	s_add_i32 s21, s21, 2
	s_barrier
	s_waitcnt lgkmcnt(11)
	v_mfma_f32_16x16x32_bf16 v[174:177], v[178:181], v[206:209], v[174:177]
	s_lshl_b32 s22, s21, 1
	s_and_b32 s22, s22, 0x60
	s_add_i32 s22, s22, s12
	s_lshl_b32 s22, s22, 6
	v_mfma_f32_16x16x32_bf16 v[170:173], v[194:197], v[206:209], v[170:173]
	s_and_b32 s22, s22, 0x3f00
	s_or_b32 s22, s22, s13
	s_lshl_b32 s23, s21, 23
	s_lshl_b32 s22, s22, 9
	v_mfma_f32_16x16x32_bf16 v[158:161], v[198:201], v[206:209], v[158:161]
	s_and_b32 s23, s23, 0x7000000
	s_or_b32 s22, s22, s23
	s_lshl_b32 s23, s21, 8
	s_and_b32 s23, s23, 0x100
	s_or_b32 s22, s22, s23
	s_or_b32 s23, s22, 0x4000
	v_mfma_f32_16x16x32_bf16 v[142:145], v[202:205], v[206:209], v[142:145]
	s_waitcnt lgkmcnt(10)
	v_mfma_f32_16x16x32_bf16 v[166:169], v[178:181], v[210:213], v[166:169]
	v_mfma_f32_16x16x32_bf16 v[162:165], v[194:197], v[210:213], v[162:165]
	v_mfma_f32_16x16x32_bf16 v[146:149], v[198:201], v[210:213], v[146:149]
	s_or_b32 s23, s22, 0x8000
	v_mfma_f32_16x16x32_bf16 v[122:125], v[202:205], v[210:213], v[122:125]
	s_waitcnt lgkmcnt(9)
	v_mfma_f32_16x16x32_bf16 v[154:157], v[178:181], v[214:217], v[154:157]
	v_mfma_f32_16x16x32_bf16 v[150:153], v[194:197], v[214:217], v[150:153]
	v_mfma_f32_16x16x32_bf16 v[130:133], v[198:201], v[214:217], v[130:133]
	s_or_b32 s23, s22, 0xc000
	v_mfma_f32_16x16x32_bf16 v[106:109], v[202:205], v[214:217], v[106:109]
	s_waitcnt lgkmcnt(8)
	v_mfma_f32_16x16x32_bf16 v[138:141], v[178:181], v[218:221], v[138:141]
	v_mfma_f32_16x16x32_bf16 v[134:137], v[194:197], v[218:221], v[134:137]
	v_mfma_f32_16x16x32_bf16 v[114:117], v[198:201], v[218:221], v[114:117]
	s_or_b32 s23, s22, 0x10000
	v_mfma_f32_16x16x32_bf16 v[90:93], v[202:205], v[218:221], v[90:93]
	s_waitcnt lgkmcnt(7)
	v_mfma_f32_16x16x32_bf16 v[126:129], v[178:181], v[222:225], v[126:129]
	v_mfma_f32_16x16x32_bf16 v[118:121], v[194:197], v[222:225], v[118:121]
	v_mfma_f32_16x16x32_bf16 v[98:101], v[198:201], v[222:225], v[98:101]
	s_or_b32 s23, s22, 0x14000
	v_mfma_f32_16x16x32_bf16 v[74:77], v[202:205], v[222:225], v[74:77]
	s_waitcnt lgkmcnt(6)
	v_mfma_f32_16x16x32_bf16 v[110:113], v[178:181], v[226:229], v[110:113]
	v_mfma_f32_16x16x32_bf16 v[102:105], v[194:197], v[226:229], v[102:105]
	v_mfma_f32_16x16x32_bf16 v[82:85], v[198:201], v[226:229], v[82:85]
	s_or_b32 s23, s22, 0x18000
	s_or_b32 s22, s22, 0x1c000
	v_mfma_f32_16x16x32_bf16 v[62:65], v[202:205], v[226:229], v[62:65]
	s_waitcnt lgkmcnt(5)
	v_mfma_f32_16x16x32_bf16 v[94:97], v[178:181], v[230:233], v[94:97]
	v_mfma_f32_16x16x32_bf16 v[86:89], v[194:197], v[230:233], v[86:89]
	v_mfma_f32_16x16x32_bf16 v[70:73], v[198:201], v[230:233], v[70:73]
	v_mfma_f32_16x16x32_bf16 v[54:57], v[202:205], v[230:233], v[54:57]
	s_waitcnt lgkmcnt(4)
	v_mfma_f32_16x16x32_bf16 v[78:81], v[178:181], v[234:237], v[78:81]
	v_mfma_f32_16x16x32_bf16 v[66:69], v[194:197], v[234:237], v[66:69]
	v_mfma_f32_16x16x32_bf16 v[58:61], v[198:201], v[234:237], v[58:61]
	v_mfma_f32_16x16x32_bf16 v[50:53], v[202:205], v[234:237], v[50:53]
	s_waitcnt lgkmcnt(0)
	s_barrier
	ds_read_b128 v[178:181], v182 offset:33792
	ds_read_b128 v[194:197], v182 offset:35840
	ds_read_b128 v[198:201], v182 offset:37888
	ds_read_b128 v[202:205], v182 offset:39936
	ds_read_b128 v[206:209], v238 offset:1024
	ds_read_b128 v[210:213], v238 offset:3072
	ds_read_b128 v[214:217], v238 offset:5120
	ds_read_b128 v[218:221], v238 offset:7168
	ds_read_b128 v[222:225], v238 offset:9216
	ds_read_b128 v[226:229], v238 offset:11264
	ds_read_b128 v[230:233], v238 offset:13312
	ds_read_b128 v[234:237], v238 offset:15360
	s_waitcnt lgkmcnt(0)
	s_barrier
	s_waitcnt lgkmcnt(11)
	v_mfma_f32_16x16x32_bf16 v[174:177], v[178:181], v[206:209], v[174:177]
	s_lshl_b32 s21, s21, 15
	s_and_b32 s21, s21, 0x78000
	s_or_b32 s21, s21, s14
	s_or_b32 s22, s21, 0x2000
	v_mfma_f32_16x16x32_bf16 v[170:173], v[194:197], v[206:209], v[170:173]
	v_mfma_f32_16x16x32_bf16 v[158:161], v[198:201], v[206:209], v[158:161]
	v_mfma_f32_16x16x32_bf16 v[142:145], v[202:205], v[206:209], v[142:145]
	s_waitcnt lgkmcnt(10)
	v_mfma_f32_16x16x32_bf16 v[166:169], v[178:181], v[210:213], v[166:169]
	v_mfma_f32_16x16x32_bf16 v[162:165], v[194:197], v[210:213], v[162:165]
	v_mfma_f32_16x16x32_bf16 v[146:149], v[198:201], v[210:213], v[146:149]
	v_mfma_f32_16x16x32_bf16 v[122:125], v[202:205], v[210:213], v[122:125]
	s_waitcnt lgkmcnt(9)
	v_mfma_f32_16x16x32_bf16 v[154:157], v[178:181], v[214:217], v[154:157]
	v_mfma_f32_16x16x32_bf16 v[150:153], v[194:197], v[214:217], v[150:153]
	v_mfma_f32_16x16x32_bf16 v[130:133], v[198:201], v[214:217], v[130:133]
	v_mfma_f32_16x16x32_bf16 v[106:109], v[202:205], v[214:217], v[106:109]
	s_waitcnt lgkmcnt(8)
	v_mfma_f32_16x16x32_bf16 v[138:141], v[178:181], v[218:221], v[138:141]
	v_mfma_f32_16x16x32_bf16 v[134:137], v[194:197], v[218:221], v[134:137]
	s_or_b32 s22, s21, 0x4000
	s_or_b32 s21, s21, 0x6000
	v_mfma_f32_16x16x32_bf16 v[114:117], v[198:201], v[218:221], v[114:117]
	v_mfma_f32_16x16x32_bf16 v[90:93], v[202:205], v[218:221], v[90:93]
	s_waitcnt lgkmcnt(7)
	v_mfma_f32_16x16x32_bf16 v[126:129], v[178:181], v[222:225], v[126:129]
	v_mfma_f32_16x16x32_bf16 v[118:121], v[194:197], v[222:225], v[118:121]
	v_mfma_f32_16x16x32_bf16 v[98:101], v[198:201], v[222:225], v[98:101]
	v_mfma_f32_16x16x32_bf16 v[74:77], v[202:205], v[222:225], v[74:77]
	s_waitcnt lgkmcnt(6)
	v_mfma_f32_16x16x32_bf16 v[110:113], v[178:181], v[226:229], v[110:113]
	v_mfma_f32_16x16x32_bf16 v[102:105], v[194:197], v[226:229], v[102:105]
	v_mfma_f32_16x16x32_bf16 v[82:85], v[198:201], v[226:229], v[82:85]
	v_mfma_f32_16x16x32_bf16 v[62:65], v[202:205], v[226:229], v[62:65]
	s_waitcnt lgkmcnt(5)
	v_mfma_f32_16x16x32_bf16 v[94:97], v[178:181], v[230:233], v[94:97]
	v_mfma_f32_16x16x32_bf16 v[86:89], v[194:197], v[230:233], v[86:89]
	v_mfma_f32_16x16x32_bf16 v[70:73], v[198:201], v[230:233], v[70:73]
	v_mfma_f32_16x16x32_bf16 v[54:57], v[202:205], v[230:233], v[54:57]
	s_waitcnt lgkmcnt(4)
	v_mfma_f32_16x16x32_bf16 v[78:81], v[178:181], v[234:237], v[78:81]
	v_mfma_f32_16x16x32_bf16 v[66:69], v[194:197], v[234:237], v[66:69]
	v_mfma_f32_16x16x32_bf16 v[58:61], v[198:201], v[234:237], v[58:61]
	v_mfma_f32_16x16x32_bf16 v[50:53], v[202:205], v[234:237], v[50:53]
	s_and_b32 s21, s18, 32
	s_add_i32 s21, s21, s12
	s_lshl_b32 s21, s21, 6
	s_and_b32 s21, s21, 0x3f00
	v_add_lshl_u32 v182, v193, s21, 9
	v_add_u32_e32 v206, v184, v182
	buffer_store_dwordx4 v[174:177], v206, s[28:31], 0 offen
	buffer_store_dwordx4 v[170:173], v206, s[28:31], 0 offen offset:64
	buffer_store_dwordx4 v[158:161], v206, s[28:31], 0 offen offset:128
	buffer_store_dwordx4 v[142:145], v206, s[28:31], 0 offen offset:192
	buffer_store_dwordx4 v[166:169], v206, s[28:31], s8 offen
	buffer_store_dwordx4 v[162:165], v206, s[28:31], s8 offen offset:64
	buffer_store_dwordx4 v[146:149], v206, s[28:31], s8 offen offset:128
	buffer_store_dwordx4 v[122:125], v206, s[28:31], s8 offen offset:192
	buffer_store_dwordx4 v[154:157], v206, s[28:31], s15 offen
	buffer_store_dwordx4 v[150:153], v206, s[28:31], s15 offen offset:64
	buffer_store_dwordx4 v[130:133], v206, s[28:31], s15 offen offset:128
	buffer_store_dwordx4 v[106:109], v206, s[28:31], s15 offen offset:192
	buffer_store_dwordx4 v[138:141], v206, s[28:31], s9 offen
	buffer_store_dwordx4 v[134:137], v206, s[28:31], s9 offen offset:64
	buffer_store_dwordx4 v[114:117], v206, s[28:31], s9 offen offset:128
	buffer_store_dwordx4 v[90:93], v206, s[28:31], s9 offen offset:192
	buffer_store_dwordx4 v[126:129], v206, s[28:31], s16 offen
	buffer_store_dwordx4 v[118:121], v206, s[28:31], s16 offen offset:64
	buffer_store_dwordx4 v[98:101], v206, s[28:31], s16 offen offset:128
	buffer_store_dwordx4 v[74:77], v206, s[28:31], s16 offen offset:192
	buffer_store_dwordx4 v[110:113], v206, s[28:31], s10 offen
	buffer_store_dwordx4 v[102:105], v206, s[28:31], s10 offen offset:64
	buffer_store_dwordx4 v[82:85], v206, s[28:31], s10 offen offset:128
	buffer_store_dwordx4 v[62:65], v206, s[28:31], s10 offen offset:192
	buffer_store_dwordx4 v[94:97], v206, s[28:31], s17 offen
	buffer_store_dwordx4 v[86:89], v206, s[28:31], s17 offen offset:64
	buffer_store_dwordx4 v[70:73], v206, s[28:31], s17 offen offset:128
	buffer_store_dwordx4 v[54:57], v206, s[28:31], s17 offen offset:192
	buffer_store_dwordx4 v[78:81], v206, s[28:31], s11 offen
	buffer_store_dwordx4 v[66:69], v206, s[28:31], s11 offen offset:64
	buffer_store_dwordx4 v[58:61], v206, s[28:31], s11 offen offset:128
	buffer_store_dwordx4 v[50:53], v206, s[28:31], s11 offen offset:192
	s_waitcnt lgkmcnt(0)
	s_barrier
	s_branch .LBB1_6
